# p1 MoE-output gather issued one pass ahead (pointers + 32 loads before the previous pass's first barrier; consuming pass skips chain and loads)
# speedup vs baseline: 1.0109x; 1.0109x over previous
; #define INP(i)  ((const float*)(const GAS float*)karg64(8 * (i)))
; #define OUTP()  ((float*)(GAS float*)karg64(232))
; #define F_CTL   ((unsigned*)(WSP() + WS_CTL))
; #define F_MOD   ((float*)(WSP() + WS_MOD))
; #define F_DT    ((float*)(WSP() + WS_DT))
; #define F_INV   ((int*)(WSP() + WS_INV))
; #define F_SAH   ((float*)(WSP() + WS_SAH))
; #define F_HAQ   ((signed char*)(WSP() + WS_HA))
; __device__ __forceinline__ void p1_norm1(const Frame& F, int layer, int probe_rerun) {
;     ...
;     const int gw = F.blk * NWAVES + F.wave, NGW = F.G * NWAVES, lane = F.lane;
;     const int nrows = fin ? NL : NT;
;     const int RW = 2 * ((nrows + 2 * NGW - 1) / (2 * NGW)), rbeg = gw * RW;
;     const float* modl = F_MOD + (size_t)(fin ? 0 : layer) * 17 * 6144;
;     const float* modp = F_MOD + (size_t)(layer > 0 ? layer - 1 : 0) * 17 * 6144;
;     const float* n1w = INP(I_N1W) + (size_t)(fin ? 0 : layer) * D;
;     float* const outp = OUTP(); bf16_t* const xb = F_XB; const bool srcf32 = (layer == 0 && !probe_rerun);
;     const float* const srcl = INP(I_X); const float* const srcc = INP(I_CTX);
;     const int* const invp = F_INV; const bf16_t* const Yp = F_Y; signed char* const HQp = F_HAQ; float* const SAp = F_SAH; float* const DTp = F_DT;
;     const bf16_t* const zrow = (const bf16_t*)(F_CTL + CW_ZERO);
;     const float* const dtbf = INP(I_DTBF) + (fin ? 0 : layer) * 8; const float* const dtbb = INP(I_DTBB) + (fin ? 0 : layer) * 8;
;     const bool comb = (layer > 0 && !probe_rerun);
;     f32x4 nva[4], nvb[4]; int nia = -1, nib = -1;
;     f32x4 W1[4], S0[4], G2[4]; int cur_m = -1;
; #pragma unroll
;     for (int j = 0; j < 4; ++j) { W1[j] = (f32x4){0.f, 0.f, 0.f, 0.f}; S0[j] = W1[j]; G2[j] = W1[j]; }
.LBB0_141:
	s_mov_b32 s62, s66
	s_mov_b32 s63, s31
	s_max_i32 s30, s66, 1
	s_add_i32 s30, s30, -1
	s_lshl_b64 s[36:37], s[62:63], 12
	s_add_u32 s52, s38, 0x44734800
	s_addc_u32 s53, s39, 0
	s_add_u32 s54, s40, 0x8000
	s_mul_i32 s57, s66, 0x66000
	s_mul_hi_u32 s60, s30, 0x66000
	s_mul_i32 s61, s30, 0x66000
	s_addc_u32 s55, s41, 0
	s_lshl_b32 s30, s66, 3
	s_mul_hi_u32 s35, s66, 0x66000
	s_add_u32 s14, s14, s57
	s_addc_u32 s15, s15, s35
	s_add_u32 s14, s14, 0x200000
	s_addc_u32 s15, s15, 0
	s_add_u32 s10, s10, s61
	s_addc_u32 s11, s11, s60
	s_add_u32 s36, s12, s36
	s_addc_u32 s37, s13, s37
	s_add_u32 s12, s16, 0x2f104800
	s_addc_u32 s13, s17, 0
	s_lshl_b64 s[16:17], s[30:31], 2
	s_add_u32 s20, s20, s16
	s_addc_u32 s21, s21, s17
	s_add_u32 s18, s18, s16
	v_and_b32_e32 v33, 15, v36
	s_addc_u32 s19, s19, s17
	v_lshlrev_b32_e32 v144, 2, v33
	v_lshl_add_u64 v[130:131], v[36:37], 2, s[28:29]
	v_cmp_eq_u32_e64 s[38:39], 0, v36
	v_lshlrev_b32_e32 v236, 3, v36
	v_and_b32_e32 v39, -16, v36
	v_lshlrev_b32_e32 v34, 4, v36
	v_lshrrev_b32_e32 v41, 4, v36
	v_lshl_add_u64 v[36:37], s[18:19], 0, v[144:145]
	s_movk_i32 s18, 0xffe0
	s_mov_b32 s19, -1
	v_and_b32_e32 v40, 0xffffff00, v34
	v_lshl_add_u64 v[34:35], s[20:21], 0, v[144:145]
	v_lshl_add_u64 v[36:37], v[36:37], 0, s[18:19]
	v_cmp_gt_u32_e32 vcc, 8, v33
	v_mul_u32_u24_e32 v38, 0x810, v33
	v_readlane_b32 s28, v254, 55
	v_cndmask_b32_e32 v139, v37, v35, vcc
	v_cndmask_b32_e32 v138, v36, v34, vcc
	v_lshl_add_u64 v[34:35], s[6:7], 0, v[144:145]
	s_mov_b64 s[6:7], 0x2c498800
	v_lshl_add_u64 v[140:141], v[34:35], 0, s[6:7]
	s_mul_i32 s6, s56, 0x1020
	v_readlane_b32 s7, v254, 54
	v_ashrrev_i32_e32 v33, 5, v32
	s_add_i32 s17, s7, s6
	s_add_i32 s18, s28, s6
	s_addk_i32 s6, 0x810
	v_add_u32_e32 v33, s58, v33
	v_readlane_b32 s21, v254, 53
	s_add_i32 s19, s7, s6
	v_add_u32_e32 v35, s7, v236
	s_lshl_b32 s7, s56, 8
	v_mul_lo_u32 v33, s59, v33
	v_add3_u32 v34, s21, v40, v144
	s_add_i32 s20, s28, s6
	v_add_u32_e32 v36, s28, v236
	v_add3_u32 v37, v38, v39, s7
	s_lshl_b32 s7, s56, 10
	v_and_or_b32 v237, v41, 1, v33
	v_lshl_add_u32 v238, v32, 2, s21
	v_lshl_add_u64 v[32:33], s[2:3], 0, v[128:129]
	s_mov_b64 s[2:3], 0x23498800
	v_mov_b32_e32 v144, v145
	v_add_u32_e32 v132, 0x100, v128
	v_add_u32_e32 v134, 0x200, v128
	v_add_u32_e32 v136, 0x300, v128
	s_cmp_lt_i32 s56, 4
	v_lshl_add_u64 v[150:151], v[32:33], 0, s[2:3]
	v_mov_b32_e32 v146, v145
	v_mov_b32_e32 v147, v145
	v_add_u32_e32 v239, s6, v35
	v_add_u32_e32 v240, s6, v36
	v_add_u32_e32 v241, 0, v37
	v_add_u32_e32 v242, s7, v34
	v_mov_b64_e32 v[76:77], v[144:145]
	v_mov_b64_e32 v[64:65], v[144:145]
	v_mov_b64_e32 v[68:69], v[144:145]
	v_mov_b64_e32 v[72:73], v[144:145]
	v_mov_b64_e32 v[60:61], v[144:145]
	v_mov_b64_e32 v[56:57], v[144:145]
	v_mov_b64_e32 v[52:53], v[144:145]
	v_mov_b64_e32 v[48:49], v[144:145]
	v_mov_b64_e32 v[32:33], v[144:145]
	v_mov_b64_e32 v[36:37], v[144:145]
	v_mov_b64_e32 v[40:41], v[144:145]
	v_mov_b64_e32 v[44:45], v[144:145]
	s_mov_b32 s34, -1
	v_ashrrev_i32_e32 v133, 31, v132
	v_ashrrev_i32_e32 v135, 31, v134
	v_ashrrev_i32_e32 v137, 31, v136
	s_mov_b32 s16, 0
	v_lshl_add_u64 v[142:143], v[128:129], 2, s[36:37]
	s_cselect_b64 s[56:57], -1, 0
	v_lshl_add_u64 v[148:149], v[128:129], 1, s[4:5]
	v_mov_b64_e32 v[78:79], v[146:147]
	v_mov_b64_e32 v[66:67], v[146:147]
	v_mov_b64_e32 v[70:71], v[146:147]
	v_mov_b64_e32 v[74:75], v[146:147]
	v_mov_b64_e32 v[62:63], v[146:147]
	v_mov_b64_e32 v[58:59], v[146:147]
	v_mov_b64_e32 v[54:55], v[146:147]
	v_mov_b64_e32 v[50:51], v[146:147]
	v_mov_b64_e32 v[34:35], v[146:147]
	v_mov_b64_e32 v[38:39], v[146:147]
	v_mov_b64_e32 v[42:43], v[146:147]
	v_mov_b64_e32 v[46:47], v[146:147]
	s_mov_b32 s97, 0
	s_branch .LBB0_143

; __device__ __forceinline__ int shl_from_i(int v, int src_lane) { return __builtin_amdgcn_ds_bpermute(src_lane << 2, v); }
; __device__ __forceinline__ void p1_gather_issue(u32x2 (&wa)[4][4], u32x2 (&wb)[4][4], unsigned& maska, unsigned& maskb, int inva, int invb, const bf16_t* Yp, const bf16_t* zrow, int lane) {
;     maska = (unsigned)__ballot(inva >= 0) & 0xffffu; maskb = (unsigned)__ballot(invb >= 0) & 0xffffu;
;     const bf16_t* ypa[4]; const bf16_t* ypb[4];
; #pragma unroll
;     for (int q = 0; q < 4; ++q) {
;         if (maska) { const int e = __builtin_ctz(maska); maska &= maska - 1; ypa[q] = Yp + (size_t)shl_from_i(inva, e) * D; } else ypa[q] = zrow;
;         if (maskb) { const int e = __builtin_ctz(maskb); maskb &= maskb - 1; ypb[q] = Yp + (size_t)shl_from_i(invb, e) * D; } else ypb[q] = zrow; }
.LBB0_166:
	s_and_b64 vcc, exec, s[40:41]
	s_or_b32 s62, s6, 1
	s_cbranch_vccnz .LBB0_205
	s_cmp_eq_u32 s97, 1
	s_cbranch_scc0 .Lp1pf_cold
	s_mov_b32 s97, 0
	s_mov_b32 s3, s99
	s_mov_b32 s2, s98
	v_lshlrev_b64 v[112:113], 1, v[128:129]
	v_mov_b32_e32 v114, 0
	v_mov_b32_e32 v115, v114
	v_mov_b32_e32 v116, v114
	v_mov_b32_e32 v117, v114
	v_mov_b32_e32 v124, v114
	v_mov_b32_e32 v125, v114
	v_mov_b32_e32 v122, v114
	v_mov_b32_e32 v123, v114
	v_mov_b32_e32 v154, v114
	v_mov_b32_e32 v155, v114
	v_mov_b32_e32 v152, v114
	v_mov_b32_e32 v153, v114
	v_mov_b32_e32 v162, v114
	v_mov_b32_e32 v163, v114
	v_mov_b32_e32 v160, v114
	v_mov_b32_e32 v161, v114
	v_mov_b32_e32 v166, v114
	v_mov_b32_e32 v167, v114
	v_mov_b32_e32 v164, v114
	v_mov_b32_e32 v165, v114
	v_mov_b32_e32 v158, v114
	v_mov_b32_e32 v159, v114
	v_mov_b32_e32 v156, v114
	v_mov_b32_e32 v157, v114
	v_mov_b32_e32 v146, v114
	v_mov_b32_e32 v147, v114
	v_mov_b32_e32 v126, v114
	v_mov_b32_e32 v127, v114
	v_mov_b32_e32 v120, v114
	v_mov_b32_e32 v121, v114
	v_mov_b32_e32 v118, v114
	v_mov_b32_e32 v119, v114
	s_branch .Lp1pf_wait
.Lp1pf_cold:
	v_cmp_lt_i32_e64 s[4:5], -1, v245
	s_and_b32 s6, s4, 0xffff
	v_cmp_lt_i32_e64 s[2:3], -1, v244
	s_mov_b32 s3, 0
	s_cmp_eq_u32 s6, 0
	v_mov_b64_e32 v[114:115], s[54:55]
	s_mov_b32 s5, 0
	s_cbranch_scc1 .LBB0_169
	s_ff1_i32_b32 s5, s6
	s_lshl_b32 s5, s5, 2
	v_mov_b32_e32 v112, s5
	ds_bpermute_b32 v112, v112, v245
	s_add_i32 s4, s4, -1
	s_and_b32 s5, s4, s6
	s_waitcnt lgkmcnt(0)
	v_ashrrev_i32_e32 v113, 31, v112
	v_lshlrev_b64 v[112:113], 11, v[112:113]
	v_lshl_add_u64 v[114:115], s[52:53], 0, v[112:113]

; __device__ __forceinline__ float bflo(unsigned w) { return __uint_as_float(w << 16); }
; __device__ __forceinline__ float bfhi(unsigned w) { return __uint_as_float(w & 0xffff0000u); }
; __device__ __forceinline__ int shl_from_i(int v, int src_lane) { return __builtin_amdgcn_ds_bpermute(src_lane << 2, v); }
; __device__ __forceinline__ void p1_gather_consume(f32x4 (&va)[4], f32x4 (&vb)[4], u32x2 (&wa)[4][4], u32x2 (&wb)[4][4], unsigned maska, unsigned maskb, int inva, int invb,
;                                                   const bf16_t* Yp, const bf16_t* zrow, const f32x4 (&g2)[4], int lane) {
;     ...
;     for (;;) {
; #pragma unroll
;         for (int q = 0; q < 4; ++q)
; #pragma unroll
;             for (int j = 0; j < 4; ++j) { aa[j] += (f32x4){bflo(wa[q][j].x), bfhi(wa[q][j].x), bflo(wa[q][j].y), bfhi(wa[q][j].y)};
;                 ab[j] += (f32x4){bflo(wb[q][j].x), bfhi(wb[q][j].x), bflo(wb[q][j].y), bfhi(wb[q][j].y)}; }
;         if (!(maska | maskb)) break;
;         const bf16_t* ypa[4]; const bf16_t* ypb[4];
; #pragma unroll
;         for (int q = 0; q < 4; ++q) {
;             if (maska) { const int e = __builtin_ctz(maska); maska &= maska - 1; ypa[q] = Yp + (size_t)shl_from_i(inva, e) * D; } else ypa[q] = zrow;
;             if (maskb) { const int e = __builtin_ctz(maskb); maskb &= maskb - 1; ypb[q] = Yp + (size_t)shl_from_i(invb, e) * D; } else ypb[q] = zrow; }
.Lp1pf_wait:
	s_waitcnt vmcnt(0) lgkmcnt(0)
	v_lshlrev_b32_e32 v178, 16, v212
	v_and_b32_e32 v179, 0xffff0000, v212
	v_pk_add_f32 v[166:167], v[166:167], v[178:179]
	v_lshlrev_b32_e32 v178, 16, v208
	v_and_b32_e32 v179, 0xffff0000, v208
	v_pk_add_f32 v[162:163], v[162:163], v[178:179]
	v_lshlrev_b32_e32 v178, 16, v198
	v_and_b32_e32 v179, 0xffff0000, v198
	v_pk_add_f32 v[158:159], v[158:159], v[178:179]
	v_lshlrev_b32_e32 v178, 16, v192
	v_and_b32_e32 v179, 0xffff0000, v192
	v_pk_add_f32 v[154:155], v[154:155], v[178:179]
	v_lshlrev_b32_e32 v178, 16, v184
	v_and_b32_e32 v179, 0xffff0000, v184
	v_pk_add_f32 v[146:147], v[146:147], v[178:179]
	v_lshlrev_b32_e32 v178, 16, v180
	v_and_b32_e32 v179, 0xffff0000, v180
	v_pk_add_f32 v[124:125], v[124:125], v[178:179]
	v_lshlrev_b32_e32 v178, 16, v172
	v_and_b32_e32 v179, 0xffff0000, v172
	v_lshlrev_b32_e32 v172, 16, v173
	v_and_b32_e32 v173, 0xffff0000, v173
	v_pk_add_f32 v[118:119], v[118:119], v[172:173]
	v_lshlrev_b32_e32 v172, 16, v170
	v_and_b32_e32 v173, 0xffff0000, v170
	v_lshlrev_b32_e32 v170, 16, v171
	v_and_b32_e32 v171, 0xffff0000, v171
	v_pk_add_f32 v[116:117], v[116:117], v[170:171]
	v_lshlrev_b32_e32 v212, 16, v213
	v_and_b32_e32 v213, 0xffff0000, v213
	v_pk_add_f32 v[164:165], v[164:165], v[212:213]
	v_lshlrev_b32_e32 v208, 16, v209
	v_and_b32_e32 v209, 0xffff0000, v209
	v_pk_add_f32 v[114:115], v[114:115], v[172:173]
	v_pk_add_f32 v[160:161], v[160:161], v[208:209]
	v_lshlrev_b32_e32 v198, 16, v199
	v_and_b32_e32 v199, 0xffff0000, v199
	v_pk_add_f32 v[156:157], v[156:157], v[198:199]
	v_lshlrev_b32_e32 v192, 16, v193
	v_and_b32_e32 v193, 0xffff0000, v193
	v_pk_add_f32 v[152:153], v[152:153], v[192:193]
	v_lshlrev_b32_e32 v184, 16, v185
	v_and_b32_e32 v185, 0xffff0000, v185
	v_pk_add_f32 v[126:127], v[126:127], v[184:185]
	v_lshlrev_b32_e32 v180, 16, v181
	v_and_b32_e32 v181, 0xffff0000, v181
	v_pk_add_f32 v[120:121], v[120:121], v[178:179]
	v_pk_add_f32 v[122:123], v[122:123], v[180:181]
	s_or_b32 s4, s3, s2
	s_cmp_eq_u32 s4, 0
	v_readfirstlane_b32 s5, v0
	v_readfirstlane_b32 s4, v0
	v_lshlrev_b32_e32 v170, 16, v226
	v_and_b32_e32 v171, 0xffff0000, v226
	v_pk_add_f32 v[166:167], v[166:167], v[170:171]
	v_lshlrev_b32_e32 v172, 16, v227
	v_and_b32_e32 v173, 0xffff0000, v227
	v_pk_add_f32 v[164:165], v[164:165], v[172:173]
	v_lshlrev_b32_e32 v170, 16, v232
	v_and_b32_e32 v171, 0xffff0000, v232
	v_pk_add_f32 v[162:163], v[162:163], v[170:171]
	v_lshlrev_b32_e32 v170, 16, v220
	v_and_b32_e32 v171, 0xffff0000, v220
	v_lshlrev_b32_e32 v172, 16, v233
	v_and_b32_e32 v173, 0xffff0000, v233
	v_pk_add_f32 v[158:159], v[158:159], v[170:171]
	v_lshlrev_b32_e32 v170, 16, v230
	v_and_b32_e32 v171, 0xffff0000, v230
	v_pk_add_f32 v[160:161], v[160:161], v[172:173]
	v_lshlrev_b32_e32 v172, 16, v221
	v_and_b32_e32 v173, 0xffff0000, v221
	v_pk_add_f32 v[154:155], v[154:155], v[170:171]
	v_lshlrev_b32_e32 v170, 16, v216
	v_and_b32_e32 v171, 0xffff0000, v216
	v_pk_add_f32 v[156:157], v[156:157], v[172:173]
	v_lshlrev_b32_e32 v172, 16, v231
	v_and_b32_e32 v173, 0xffff0000, v231
	v_pk_add_f32 v[146:147], v[146:147], v[170:171]
	v_lshlrev_b32_e32 v170, 16, v228
	v_and_b32_e32 v171, 0xffff0000, v228
	v_pk_add_f32 v[152:153], v[152:153], v[172:173]
	v_lshlrev_b32_e32 v172, 16, v217
	v_and_b32_e32 v173, 0xffff0000, v217
	v_pk_add_f32 v[124:125], v[124:125], v[170:171]
	v_lshlrev_b32_e32 v170, 16, v210
	v_and_b32_e32 v171, 0xffff0000, v210
	v_pk_add_f32 v[126:127], v[126:127], v[172:173]
	v_lshlrev_b32_e32 v172, 16, v229
	v_and_b32_e32 v173, 0xffff0000, v229
	v_pk_add_f32 v[120:121], v[120:121], v[170:171]
	v_lshlrev_b32_e32 v170, 16, v224
	v_and_b32_e32 v171, 0xffff0000, v224
	v_pk_add_f32 v[122:123], v[122:123], v[172:173]
	v_lshlrev_b32_e32 v172, 16, v211
	v_and_b32_e32 v173, 0xffff0000, v211
	v_pk_add_f32 v[114:115], v[114:115], v[170:171]
	v_lshlrev_b32_e32 v170, 16, v206
	v_and_b32_e32 v171, 0xffff0000, v206
	v_pk_add_f32 v[118:119], v[118:119], v[172:173]
	v_lshlrev_b32_e32 v172, 16, v225
	v_and_b32_e32 v173, 0xffff0000, v225
	v_pk_add_f32 v[166:167], v[166:167], v[170:171]
	v_lshlrev_b32_e32 v170, 16, v222
	v_and_b32_e32 v171, 0xffff0000, v222
; __device__ __forceinline__ float bflo(unsigned w) { return __uint_as_float(w << 16); }
; __device__ __forceinline__ float bfhi(unsigned w) { return __uint_as_float(w & 0xffff0000u); }
; __device__ __forceinline__ int shl_from_i(int v, int src_lane) { return __builtin_amdgcn_ds_bpermute(src_lane << 2, v); }
; __device__ __forceinline__ void p1_gather_consume(f32x4 (&va)[4], f32x4 (&vb)[4], u32x2 (&wa)[4][4], u32x2 (&wb)[4][4], unsigned maska, unsigned maskb, int inva, int invb,
;                                                   const bf16_t* Yp, const bf16_t* zrow, const f32x4 (&g2)[4], int lane) {
;     ...
;         for (int q = 0; q < 4; ++q)
; #pragma unroll
;             for (int j = 0; j < 4; ++j) { aa[j] += (f32x4){bflo(wa[q][j].x), bfhi(wa[q][j].x), bflo(wa[q][j].y), bfhi(wa[q][j].y)};
;                 ab[j] += (f32x4){bflo(wb[q][j].x), bfhi(wb[q][j].x), bflo(wb[q][j].y), bfhi(wb[q][j].y)}; }
;         if (!(maska | maskb)) break;
;         const bf16_t* ypa[4]; const bf16_t* ypb[4];
; #pragma unroll
;         for (int q = 0; q < 4; ++q) {
;             if (maska) { const int e = __builtin_ctz(maska); maska &= maska - 1; ypa[q] = Yp + (size_t)shl_from_i(inva, e) * D; } else ypa[q] = zrow;
;             if (maskb) { const int e = __builtin_ctz(maskb); maskb &= maskb - 1; ypb[q] = Yp + (size_t)shl_from_i(invb, e) * D; } else ypb[q] = zrow; }
	v_pk_add_f32 v[116:117], v[116:117], v[172:173]
	v_lshlrev_b32_e32 v172, 16, v207
	v_and_b32_e32 v173, 0xffff0000, v207
	v_pk_add_f32 v[162:163], v[162:163], v[170:171]
	v_lshlrev_b32_e32 v170, 16, v200
	v_and_b32_e32 v171, 0xffff0000, v200
	v_pk_add_f32 v[164:165], v[164:165], v[172:173]
	v_lshlrev_b32_e32 v172, 16, v223
	v_and_b32_e32 v173, 0xffff0000, v223
	v_pk_add_f32 v[158:159], v[158:159], v[170:171]
	v_lshlrev_b32_e32 v170, 16, v218
	v_and_b32_e32 v171, 0xffff0000, v218
	v_pk_add_f32 v[160:161], v[160:161], v[172:173]
	v_lshlrev_b32_e32 v172, 16, v201
	v_and_b32_e32 v173, 0xffff0000, v201
	v_pk_add_f32 v[154:155], v[154:155], v[170:171]
	v_lshlrev_b32_e32 v170, 16, v194
	v_and_b32_e32 v171, 0xffff0000, v194
	v_pk_add_f32 v[156:157], v[156:157], v[172:173]
	v_lshlrev_b32_e32 v172, 16, v219
	v_and_b32_e32 v173, 0xffff0000, v219
	v_pk_add_f32 v[146:147], v[146:147], v[170:171]
	v_lshlrev_b32_e32 v170, 16, v214
	v_and_b32_e32 v171, 0xffff0000, v214
	v_pk_add_f32 v[152:153], v[152:153], v[172:173]
	v_lshlrev_b32_e32 v172, 16, v195
	v_and_b32_e32 v173, 0xffff0000, v195
	v_pk_add_f32 v[124:125], v[124:125], v[170:171]
	v_lshlrev_b32_e32 v170, 16, v190
	v_and_b32_e32 v171, 0xffff0000, v190
	v_pk_add_f32 v[126:127], v[126:127], v[172:173]
	v_lshlrev_b32_e32 v172, 16, v215
	v_and_b32_e32 v173, 0xffff0000, v215
	v_pk_add_f32 v[120:121], v[120:121], v[170:171]
	v_lshlrev_b32_e32 v170, 16, v204
	v_and_b32_e32 v171, 0xffff0000, v204
	v_pk_add_f32 v[122:123], v[122:123], v[172:173]
	v_lshlrev_b32_e32 v172, 16, v191
	v_and_b32_e32 v173, 0xffff0000, v191
	v_pk_add_f32 v[114:115], v[114:115], v[170:171]
	v_lshlrev_b32_e32 v170, 16, v186
	v_and_b32_e32 v171, 0xffff0000, v186
	v_pk_add_f32 v[118:119], v[118:119], v[172:173]
	v_lshlrev_b32_e32 v172, 16, v205
	v_and_b32_e32 v173, 0xffff0000, v205
	v_pk_add_f32 v[166:167], v[166:167], v[170:171]
	v_lshlrev_b32_e32 v170, 16, v202
	v_and_b32_e32 v171, 0xffff0000, v202
	v_pk_add_f32 v[116:117], v[116:117], v[172:173]
	v_lshlrev_b32_e32 v172, 16, v187
	v_and_b32_e32 v173, 0xffff0000, v187
	v_pk_add_f32 v[162:163], v[162:163], v[170:171]
	v_lshlrev_b32_e32 v170, 16, v176
	v_and_b32_e32 v171, 0xffff0000, v176
	v_pk_add_f32 v[164:165], v[164:165], v[172:173]
	v_lshlrev_b32_e32 v172, 16, v203
	v_and_b32_e32 v173, 0xffff0000, v203
	v_pk_add_f32 v[158:159], v[158:159], v[170:171]
	v_lshlrev_b32_e32 v170, 16, v196
	v_and_b32_e32 v171, 0xffff0000, v196
	v_pk_add_f32 v[160:161], v[160:161], v[172:173]
	v_lshlrev_b32_e32 v172, 16, v177
	v_and_b32_e32 v173, 0xffff0000, v177
	v_pk_add_f32 v[154:155], v[154:155], v[170:171]
	v_lshlrev_b32_e32 v170, 16, v174
	v_and_b32_e32 v171, 0xffff0000, v174
	v_pk_add_f32 v[156:157], v[156:157], v[172:173]
	v_lshlrev_b32_e32 v172, 16, v197
	v_and_b32_e32 v173, 0xffff0000, v197
	v_pk_add_f32 v[146:147], v[146:147], v[170:171]
	v_lshlrev_b32_e32 v170, 16, v188
	v_and_b32_e32 v171, 0xffff0000, v188
	v_pk_add_f32 v[152:153], v[152:153], v[172:173]
	v_lshlrev_b32_e32 v172, 16, v175
	v_and_b32_e32 v173, 0xffff0000, v175
	v_pk_add_f32 v[124:125], v[124:125], v[170:171]
	v_lshlrev_b32_e32 v170, 16, v168
	v_and_b32_e32 v171, 0xffff0000, v168
	v_lshlrev_b32_e32 v168, 16, v169
	v_and_b32_e32 v169, 0xffff0000, v169
	v_pk_add_f32 v[126:127], v[126:127], v[172:173]
	v_lshlrev_b32_e32 v172, 16, v189
	v_and_b32_e32 v173, 0xffff0000, v189
	v_pk_add_f32 v[118:119], v[118:119], v[168:169]
	v_pk_add_f32 v[120:121], v[120:121], v[170:171]
	v_lshlrev_b32_e32 v168, 16, v182
	v_and_b32_e32 v169, 0xffff0000, v182
	v_lshlrev_b32_e32 v170, 16, v183
	v_and_b32_e32 v171, 0xffff0000, v183
	v_pk_add_f32 v[122:123], v[122:123], v[172:173]
	v_pk_add_f32 v[116:117], v[116:117], v[170:171]
	v_pk_add_f32 v[114:115], v[114:115], v[168:169]
	s_cbranch_scc1 .LBB0_184
	s_mov_b32 s4, 0
	s_cmp_eq_u32 s3, 0
	v_mov_b64_e32 v[170:171], s[54:55]
	s_mov_b32 s5, 0
	s_cbranch_scc1 .LBB0_188
	s_ff1_i32_b32 s5, s3
	s_lshl_b32 s5, s5, 2
	v_mov_b32_e32 v168, s5
	ds_bpermute_b32 v168, v168, v245
	s_add_i32 s5, s3, -1
	s_and_b32 s5, s5, s3
	s_waitcnt lgkmcnt(0)
	v_ashrrev_i32_e32 v169, 31, v168
	v_lshlrev_b64 v[168:169], 11, v[168:169]
	v_lshl_add_u64 v[170:171], s[52:53], 0, v[168:169]

; #define LAS __attribute__((address_space(3)))
; __device__ __forceinline__ unsigned pk2(float lo, float hi) { f32x2_t v = {lo, hi}; bf16x2_t b = __builtin_convertvector(v, bf16x2_t); return __builtin_bit_cast(unsigned, b); }
; __device__ __forceinline__ float bflo(unsigned w) { return __uint_as_float(w << 16); }
; __device__ __forceinline__ float bfhi(unsigned w) { return __uint_as_float(w & 0xffff0000u); }
; __device__ __forceinline__ int shl_from_i(int v, int src_lane) { return __builtin_amdgcn_ds_bpermute(src_lane << 2, v); }
; __device__ __forceinline__ void thin_stage_row(LAS unsigned char* L, int srow, const f32x4 (&h)[4], int lane) {
; #pragma unroll
;     for (int j = 0; j < 4; ++j) { const int k = 4 * (lane + 64 * j);
;         const u32x2 hi = {pk2(h[j][0], h[j][1]), pk2(h[j][2], h[j][3])};
;         const u32x2 lo = {pk2(h[j][0] - bflo(hi.x), h[j][1] - bfhi(hi.x)), pk2(h[j][2] - bflo(hi.y), h[j][3] - bfhi(hi.y))};
;         *(LAS u32x2*)(L + TH_HHI + srow * TH_STR + k * 2) = hi; *(LAS u32x2*)(L + TH_HLO + srow * TH_STR + k * 2) = lo; }
; }
; __device__ __forceinline__ void p1_gather_issue(u32x2 (&wa)[4][4], u32x2 (&wb)[4][4], unsigned& maska, unsigned& maskb, int inva, int invb, const bf16_t* Yp, const bf16_t* zrow, int lane) {
;     maska = (unsigned)__ballot(inva >= 0) & 0xffffu; maskb = (unsigned)__ballot(invb >= 0) & 0xffffu;
;     const bf16_t* ypa[4]; const bf16_t* ypb[4];
; #pragma unroll
;     for (int q = 0; q < 4; ++q) {
;         if (maska) { const int e = __builtin_ctz(maska); maska &= maska - 1; ypa[q] = Yp + (size_t)shl_from_i(inva, e) * D; } else ypa[q] = zrow;
;         if (maskb) { const int e = __builtin_ctz(maskb); maskb &= maskb - 1; ypb[q] = Yp + (size_t)shl_from_i(invb, e) * D; } else ypb[q] = zrow; }
.LBB0_209:
	v_cvt_pk_bf16_f32 v96, v114, v115
	v_cvt_pk_bf16_f32 v97, v112, v113
	v_lshlrev_b32_e32 v98, 16, v96
	v_and_b32_e32 v99, 0xffff0000, v96
	v_pk_add_f32 v[98:99], v[114:115], v[98:99] neg_lo:[0,1] neg_hi:[0,1]
	v_lshlrev_b32_e32 v114, 16, v97
	v_and_b32_e32 v115, 0xffff0000, v97
	v_pk_add_f32 v[112:113], v[112:113], v[114:115] neg_lo:[0,1] neg_hi:[0,1]
	v_cvt_pk_bf16_f32 v98, v98, v99
	v_cvt_pk_bf16_f32 v99, v112, v113
	v_cvt_pk_bf16_f32 v112, v110, v111
	v_cvt_pk_bf16_f32 v113, v108, v109
	v_lshlrev_b32_e32 v114, 16, v112
	v_and_b32_e32 v115, 0xffff0000, v112
	v_pk_add_f32 v[110:111], v[110:111], v[114:115] neg_lo:[0,1] neg_hi:[0,1]
	v_lshlrev_b32_e32 v114, 16, v113
	v_and_b32_e32 v115, 0xffff0000, v113
	v_add_u32_e32 v116, s17, v236
	v_pk_add_f32 v[108:109], v[108:109], v[114:115] neg_lo:[0,1] neg_hi:[0,1]
	v_add_u32_e32 v117, s18, v236
	v_cvt_pk_bf16_f32 v110, v110, v111
	v_cvt_pk_bf16_f32 v111, v108, v109
	ds_write2st64_b64 v116, v[96:97], v[112:113] offset1:1
	ds_write2st64_b64 v117, v[98:99], v[110:111] offset1:1
	v_cvt_pk_bf16_f32 v96, v106, v107
	v_cvt_pk_bf16_f32 v97, v104, v105
	v_lshlrev_b32_e32 v98, 16, v96
	v_and_b32_e32 v99, 0xffff0000, v96
	v_pk_add_f32 v[98:99], v[106:107], v[98:99] neg_lo:[0,1] neg_hi:[0,1]
	v_lshlrev_b32_e32 v106, 16, v97
	v_and_b32_e32 v107, 0xffff0000, v97
	v_pk_add_f32 v[104:105], v[104:105], v[106:107] neg_lo:[0,1] neg_hi:[0,1]
	v_cvt_pk_bf16_f32 v98, v98, v99
	v_cvt_pk_bf16_f32 v99, v104, v105
	v_cvt_pk_bf16_f32 v104, v102, v103
	v_cvt_pk_bf16_f32 v105, v100, v101
	v_lshlrev_b32_e32 v106, 16, v104
	v_and_b32_e32 v107, 0xffff0000, v104
	v_pk_add_f32 v[102:103], v[102:103], v[106:107] neg_lo:[0,1] neg_hi:[0,1]
	v_lshlrev_b32_e32 v106, 16, v105
	v_and_b32_e32 v107, 0xffff0000, v105
	v_pk_add_f32 v[100:101], v[100:101], v[106:107] neg_lo:[0,1] neg_hi:[0,1]
	v_cvt_pk_bf16_f32 v102, v102, v103
	v_cvt_pk_bf16_f32 v103, v100, v101
	ds_write2st64_b64 v116, v[96:97], v[104:105] offset0:2 offset1:3
	ds_write2st64_b64 v117, v[98:99], v[102:103] offset0:2 offset1:3
	v_cvt_pk_bf16_f32 v96, v94, v95
	v_cvt_pk_bf16_f32 v97, v92, v93
	v_lshlrev_b32_e32 v98, 16, v96
	v_and_b32_e32 v99, 0xffff0000, v96
	v_pk_add_f32 v[94:95], v[94:95], v[98:99] neg_lo:[0,1] neg_hi:[0,1]
	v_lshlrev_b32_e32 v98, 16, v97
	v_and_b32_e32 v99, 0xffff0000, v97
	v_pk_add_f32 v[92:93], v[92:93], v[98:99] neg_lo:[0,1] neg_hi:[0,1]
	v_cvt_pk_bf16_f32 v94, v94, v95
	v_cvt_pk_bf16_f32 v95, v92, v93
	v_cvt_pk_bf16_f32 v92, v90, v91
	ds_write_b64 v239, v[96:97]
	ds_write_b64 v240, v[94:95]
	v_cvt_pk_bf16_f32 v93, v88, v89
	v_lshlrev_b32_e32 v94, 16, v92
	v_and_b32_e32 v95, 0xffff0000, v92
	v_pk_add_f32 v[90:91], v[90:91], v[94:95] neg_lo:[0,1] neg_hi:[0,1]
	v_lshlrev_b32_e32 v94, 16, v93
	v_and_b32_e32 v95, 0xffff0000, v93
	v_pk_add_f32 v[88:89], v[88:89], v[94:95] neg_lo:[0,1] neg_hi:[0,1]
	v_cvt_pk_bf16_f32 v90, v90, v91
	v_cvt_pk_bf16_f32 v91, v88, v89
	v_cvt_pk_bf16_f32 v88, v86, v87
	v_cvt_pk_bf16_f32 v89, v84, v85
	v_lshlrev_b32_e32 v94, 16, v88
	v_and_b32_e32 v95, 0xffff0000, v88
	v_pk_add_f32 v[86:87], v[86:87], v[94:95] neg_lo:[0,1] neg_hi:[0,1]
	v_lshlrev_b32_e32 v94, 16, v89
	v_and_b32_e32 v95, 0xffff0000, v89
	v_pk_add_f32 v[84:85], v[84:85], v[94:95] neg_lo:[0,1] neg_hi:[0,1]
	v_add_u32_e32 v96, s19, v236
	v_cvt_pk_bf16_f32 v86, v86, v87
	v_cvt_pk_bf16_f32 v87, v84, v85
	v_cvt_pk_bf16_f32 v84, v82, v83
	v_add_u32_e32 v97, s20, v236
	ds_write2st64_b64 v96, v[92:93], v[88:89] offset0:1 offset1:2
	ds_write2st64_b64 v97, v[90:91], v[86:87] offset0:1 offset1:2
	v_cvt_pk_bf16_f32 v85, v80, v81
	v_lshlrev_b32_e32 v86, 16, v84
	v_and_b32_e32 v87, 0xffff0000, v84
	v_pk_add_f32 v[82:83], v[82:83], v[86:87] neg_lo:[0,1] neg_hi:[0,1]
	v_lshlrev_b32_e32 v86, 16, v85
	v_and_b32_e32 v87, 0xffff0000, v85
	v_pk_add_f32 v[80:81], v[80:81], v[86:87] neg_lo:[0,1] neg_hi:[0,1]
	v_cvt_pk_bf16_f32 v82, v82, v83
	v_cvt_pk_bf16_f32 v83, v80, v81
	ds_write_b64 v96, v[84:85] offset:1536
	ds_write_b64 v97, v[82:83] offset:1536
	s_cmp_eq_u64 s[48:49], 0
	s_cbranch_scc1 .Lp1pf_skip
	s_cmp_ge_i32 s16, s64
	s_cbranch_scc1 .Lp1pf_skip
	v_cmp_lt_i32_e64 s[68:69], -1, v243
	v_cmp_lt_i32_e64 s[70:71], -1, v144
	s_and_b32 s72, s68, 0xffff
	s_and_b32 s76, s70, 0xffff
	s_ff1_i32_b32 s90, s72
	s_add_i32 s73, s72, -1
	s_and_b32 s73, s73, s72
	s_lshl_b32 s90, s90, 2
	s_ff1_i32_b32 s91, s73
	s_add_i32 s74, s73, -1
	s_and_b32 s74, s74, s73
	s_lshl_b32 s91, s91, 2
	s_ff1_i32_b32 s92, s74
	s_add_i32 s75, s74, -1
	s_and_b32 s75, s75, s74
	s_lshl_b32 s92, s92, 2
	s_ff1_i32_b32 s93, s75
	s_add_i32 s99, s75, -1
	s_and_b32 s99, s99, s75
	s_lshl_b32 s93, s93, 2
	s_ff1_i32_b32 s94, s76
	s_add_i32 s67, s76, -1
	s_and_b32 s67, s67, s76
	s_lshl_b32 s94, s94, 2
	s_ff1_i32_b32 s95, s67
	s_add_i32 s88, s67, -1
	s_and_b32 s88, s88, s67
	s_lshl_b32 s95, s95, 2
	s_ff1_i32_b32 s96, s88
	s_add_i32 s89, s88, -1
	s_and_b32 s89, s89, s88
	s_lshl_b32 s96, s96, 2
	s_ff1_i32_b32 s68, s89
	s_add_i32 s98, s89, -1
	s_and_b32 s98, s98, s89
	s_lshl_b32 s68, s68, 2
	v_mov_b32_e32 v112, s90
	ds_bpermute_b32 v114, v112, v243
	v_mov_b32_e32 v113, s94
	ds_bpermute_b32 v116, v113, v144
	v_mov_b32_e32 v112, s91
	ds_bpermute_b32 v174, v112, v243
	v_mov_b32_e32 v113, s95
	ds_bpermute_b32 v168, v113, v144
	v_mov_b32_e32 v112, s92
	ds_bpermute_b32 v176, v112, v243
	v_mov_b32_e32 v113, s96
	ds_bpermute_b32 v182, v113, v144
	v_mov_b32_e32 v112, s93
	ds_bpermute_b32 v186, v112, v243
	v_mov_b32_e32 v113, s68
	ds_bpermute_b32 v188, v113, v144
	s_waitcnt lgkmcnt(0)
	s_cmp_eq_u32 s72, 0
	s_cbranch_scc1 .Lp1pf_e0
	v_ashrrev_i32_e32 v115, 31, v114
	v_lshlrev_b64 v[114:115], 11, v[114:115]
	v_lshl_add_u64 v[114:115], s[52:53], 0, v[114:115]
	s_branch .Lp1pf_n0

; __device__ __forceinline__ int shl_from_i(int v, int src_lane) { return __builtin_amdgcn_ds_bpermute(src_lane << 2, v); }
; __device__ __forceinline__ void p1_gather_issue(u32x2 (&wa)[4][4], u32x2 (&wb)[4][4], unsigned& maska, unsigned& maskb, int inva, int invb, const bf16_t* Yp, const bf16_t* zrow, int lane) {
;     ...
;         if (maska) { const int e = __builtin_ctz(maska); maska &= maska - 1; ypa[q] = Yp + (size_t)shl_from_i(inva, e) * D; } else ypa[q] = zrow;
;         if (maskb) { const int e = __builtin_ctz(maskb); maskb &= maskb - 1; ypb[q] = Yp + (size_t)shl_from_i(invb, e) * D; } else ypb[q] = zrow; }
.Lp1pf_n0:
	s_cmp_eq_u32 s76, 0
	s_cbranch_scc1 .Lp1pf_e1
	v_ashrrev_i32_e32 v117, 31, v116
	v_lshlrev_b64 v[116:117], 11, v[116:117]
	v_lshl_add_u64 v[116:117], s[52:53], 0, v[116:117]
	s_branch .Lp1pf_n1

; __device__ __forceinline__ int shl_from_i(int v, int src_lane) { return __builtin_amdgcn_ds_bpermute(src_lane << 2, v); }
; __device__ __forceinline__ void p1_gather_issue(u32x2 (&wa)[4][4], u32x2 (&wb)[4][4], unsigned& maska, unsigned& maskb, int inva, int invb, const bf16_t* Yp, const bf16_t* zrow, int lane) {
;     ...
;         if (maska) { const int e = __builtin_ctz(maska); maska &= maska - 1; ypa[q] = Yp + (size_t)shl_from_i(inva, e) * D; } else ypa[q] = zrow;
;         if (maskb) { const int e = __builtin_ctz(maskb); maskb &= maskb - 1; ypb[q] = Yp + (size_t)shl_from_i(invb, e) * D; } else ypb[q] = zrow; }
.Lp1pf_n1:
	s_cmp_eq_u32 s73, 0
	s_cbranch_scc1 .Lp1pf_e2
	v_ashrrev_i32_e32 v175, 31, v174
	v_lshlrev_b64 v[174:175], 11, v[174:175]
	v_lshl_add_u64 v[174:175], s[52:53], 0, v[174:175]
	s_branch .Lp1pf_n2

; __device__ __forceinline__ int shl_from_i(int v, int src_lane) { return __builtin_amdgcn_ds_bpermute(src_lane << 2, v); }
; __device__ __forceinline__ void p1_gather_issue(u32x2 (&wa)[4][4], u32x2 (&wb)[4][4], unsigned& maska, unsigned& maskb, int inva, int invb, const bf16_t* Yp, const bf16_t* zrow, int lane) {
;     ...
;         if (maska) { const int e = __builtin_ctz(maska); maska &= maska - 1; ypa[q] = Yp + (size_t)shl_from_i(inva, e) * D; } else ypa[q] = zrow;
;         if (maskb) { const int e = __builtin_ctz(maskb); maskb &= maskb - 1; ypb[q] = Yp + (size_t)shl_from_i(invb, e) * D; } else ypb[q] = zrow; }
.Lp1pf_n2:
	s_cmp_eq_u32 s67, 0
	s_cbranch_scc1 .Lp1pf_e3
	v_ashrrev_i32_e32 v169, 31, v168
	v_lshlrev_b64 v[168:169], 11, v[168:169]
	v_lshl_add_u64 v[168:169], s[52:53], 0, v[168:169]
	s_branch .Lp1pf_n3

; __device__ __forceinline__ int shl_from_i(int v, int src_lane) { return __builtin_amdgcn_ds_bpermute(src_lane << 2, v); }
; __device__ __forceinline__ void p1_gather_issue(u32x2 (&wa)[4][4], u32x2 (&wb)[4][4], unsigned& maska, unsigned& maskb, int inva, int invb, const bf16_t* Yp, const bf16_t* zrow, int lane) {
;     ...
;         if (maska) { const int e = __builtin_ctz(maska); maska &= maska - 1; ypa[q] = Yp + (size_t)shl_from_i(inva, e) * D; } else ypa[q] = zrow;
;         if (maskb) { const int e = __builtin_ctz(maskb); maskb &= maskb - 1; ypb[q] = Yp + (size_t)shl_from_i(invb, e) * D; } else ypb[q] = zrow; }
.Lp1pf_n3:
	s_cmp_eq_u32 s74, 0
	s_cbranch_scc1 .Lp1pf_e4
	v_ashrrev_i32_e32 v177, 31, v176
	v_lshlrev_b64 v[176:177], 11, v[176:177]
	v_lshl_add_u64 v[176:177], s[52:53], 0, v[176:177]
	s_branch .Lp1pf_n4

; __device__ __forceinline__ int shl_from_i(int v, int src_lane) { return __builtin_amdgcn_ds_bpermute(src_lane << 2, v); }
; __device__ __forceinline__ void p1_gather_issue(u32x2 (&wa)[4][4], u32x2 (&wb)[4][4], unsigned& maska, unsigned& maskb, int inva, int invb, const bf16_t* Yp, const bf16_t* zrow, int lane) {
;     ...
;         if (maska) { const int e = __builtin_ctz(maska); maska &= maska - 1; ypa[q] = Yp + (size_t)shl_from_i(inva, e) * D; } else ypa[q] = zrow;
;         if (maskb) { const int e = __builtin_ctz(maskb); maskb &= maskb - 1; ypb[q] = Yp + (size_t)shl_from_i(invb, e) * D; } else ypb[q] = zrow; }
.Lp1pf_n4:
	s_cmp_eq_u32 s88, 0
	s_cbranch_scc1 .Lp1pf_e5
	v_ashrrev_i32_e32 v183, 31, v182
	v_lshlrev_b64 v[182:183], 11, v[182:183]
	v_lshl_add_u64 v[182:183], s[52:53], 0, v[182:183]
	s_branch .Lp1pf_n5

; __device__ __forceinline__ int shl_from_i(int v, int src_lane) { return __builtin_amdgcn_ds_bpermute(src_lane << 2, v); }
; __device__ __forceinline__ void p1_gather_issue(u32x2 (&wa)[4][4], u32x2 (&wb)[4][4], unsigned& maska, unsigned& maskb, int inva, int invb, const bf16_t* Yp, const bf16_t* zrow, int lane) {
;     ...
;         if (maska) { const int e = __builtin_ctz(maska); maska &= maska - 1; ypa[q] = Yp + (size_t)shl_from_i(inva, e) * D; } else ypa[q] = zrow;
;         if (maskb) { const int e = __builtin_ctz(maskb); maskb &= maskb - 1; ypb[q] = Yp + (size_t)shl_from_i(invb, e) * D; } else ypb[q] = zrow; }
.Lp1pf_n5:
	s_cmp_eq_u32 s75, 0
	s_cbranch_scc1 .Lp1pf_e6
	v_ashrrev_i32_e32 v187, 31, v186
	v_lshlrev_b64 v[186:187], 11, v[186:187]
	v_lshl_add_u64 v[186:187], s[52:53], 0, v[186:187]
	s_branch .Lp1pf_n6

; __device__ __forceinline__ int shl_from_i(int v, int src_lane) { return __builtin_amdgcn_ds_bpermute(src_lane << 2, v); }
; __device__ __forceinline__ void p1_gather_issue(u32x2 (&wa)[4][4], u32x2 (&wb)[4][4], unsigned& maska, unsigned& maskb, int inva, int invb, const bf16_t* Yp, const bf16_t* zrow, int lane) {
;     ...
;         if (maska) { const int e = __builtin_ctz(maska); maska &= maska - 1; ypa[q] = Yp + (size_t)shl_from_i(inva, e) * D; } else ypa[q] = zrow;
;         if (maskb) { const int e = __builtin_ctz(maskb); maskb &= maskb - 1; ypb[q] = Yp + (size_t)shl_from_i(invb, e) * D; } else ypb[q] = zrow; }
.Lp1pf_n6:
	s_cmp_eq_u32 s89, 0
	s_cbranch_scc1 .Lp1pf_e7
	v_ashrrev_i32_e32 v189, 31, v188
	v_lshlrev_b64 v[188:189], 11, v[188:189]
	v_lshl_add_u64 v[188:189], s[52:53], 0, v[188:189]
	s_branch .Lp1pf_n7

; __device__ __forceinline__ int shl_from_i(int v, int src_lane) { return __builtin_amdgcn_ds_bpermute(src_lane << 2, v); }
; __device__ __forceinline__ void lds_barrier() { asm volatile("s_waitcnt lgkmcnt(0)" ::: "memory"); __builtin_amdgcn_s_barrier(); asm volatile("" ::: "memory"); }
; __device__ __forceinline__ float softplus_f(float x) { const float e = __expf(-fabsf(x)), u = 1.f + e; const float l = (u == 1.f) ? e : __logf(u) * (e * __builtin_amdgcn_rcpf(u - 1.f)); return fmaxf(x, 0.f) + l; }
; __device__ __forceinline__ void p1_gather_issue(u32x2 (&wa)[4][4], u32x2 (&wb)[4][4], unsigned& maska, unsigned& maskb, int inva, int invb, const bf16_t* Yp, const bf16_t* zrow, int lane) {
;     ...
;         if (maskb) { const int e = __builtin_ctz(maskb); maskb &= maskb - 1; ypb[q] = Yp + (size_t)shl_from_i(invb, e) * D; } else ypb[q] = zrow; }
; #pragma unroll
;     for (int q = 0; q < 4; ++q)
; #pragma unroll
;         for (int j = 0; j < 4; ++j) { wa[q][j] = *(const u32x2*)(ypa[q] + 4 * (lane + 64 * j)); wb[q][j] = *(const u32x2*)(ypb[q] + 4 * (lane + 64 * j)); }
; }
; __device__ __forceinline__ void p1_norm1(const Frame& F, int layer, int probe_rerun) {
;     ...
;         lds_barrier();
;         thin_mfma_partial(F.lds, F.wave, lane);
;         lds_barrier();
;         if (F.wave < 4) { const int t16 = F.wave * 64 + lane, srow = t16 >> 4, c = t16 & 15; const float tot = thin_total(F.lds, t16);
;             const float bias = (c < 8) ? dtbf[c] : dtbb[c - 8]; const int grow = (F.blk * NWAVES + (srow >> 1)) * RW + 2 * pi + (srow & 1);
;             if (grow < nrows) DTp[(size_t)grow * 16 + c] = softplus_f(tot + bias); }
.Lp1pf_n7:
	v_lshlrev_b64 v[112:113], 1, v[128:129]
	v_lshl_add_u64 v[114:115], v[114:115], 0, v[112:113]
	v_lshl_add_u64 v[116:117], v[116:117], 0, v[112:113]
	global_load_dwordx2 v[212:213], v[114:115], off
	global_load_dwordx2 v[198:199], v[114:115], off offset:512
	global_load_dwordx2 v[184:185], v[114:115], off offset:1024
	global_load_dwordx2 v[172:173], v[114:115], off offset:1536
	global_load_dwordx2 v[208:209], v[116:117], off
	global_load_dwordx2 v[192:193], v[116:117], off offset:512
	global_load_dwordx2 v[180:181], v[116:117], off offset:1024
	global_load_dwordx2 v[170:171], v[116:117], off offset:1536
	v_lshl_add_u64 v[174:175], v[174:175], 0, v[112:113]
	global_load_dwordx2 v[226:227], v[174:175], off
	global_load_dwordx2 v[220:221], v[174:175], off offset:512
	global_load_dwordx2 v[216:217], v[174:175], off offset:1024
	global_load_dwordx2 v[210:211], v[174:175], off offset:1536
	v_lshl_add_u64 v[174:175], v[176:177], 0, v[112:113]
	v_lshl_add_u64 v[178:179], v[186:187], 0, v[112:113]
	v_lshl_add_u64 v[168:169], v[168:169], 0, v[112:113]
	global_load_dwordx2 v[206:207], v[174:175], off
	global_load_dwordx2 v[200:201], v[174:175], off offset:512
	global_load_dwordx2 v[194:195], v[174:175], off offset:1024
	global_load_dwordx2 v[190:191], v[174:175], off offset:1536
	global_load_dwordx2 v[186:187], v[178:179], off
	global_load_dwordx2 v[176:177], v[178:179], off offset:512
	s_nop 0
	global_load_dwordx2 v[174:175], v[178:179], off offset:1024
	global_load_dwordx2 v[232:233], v[168:169], off
	global_load_dwordx2 v[230:231], v[168:169], off offset:512
	global_load_dwordx2 v[228:229], v[168:169], off offset:1024
	global_load_dwordx2 v[224:225], v[168:169], off offset:1536
	v_lshl_add_u64 v[168:169], v[182:183], 0, v[112:113]
	global_load_dwordx2 v[222:223], v[168:169], off
	global_load_dwordx2 v[218:219], v[168:169], off offset:512
	global_load_dwordx2 v[214:215], v[168:169], off offset:1024
	global_load_dwordx2 v[204:205], v[168:169], off offset:1536
	s_nop 0
	global_load_dwordx2 v[168:169], v[178:179], off offset:1536
	v_lshl_add_u64 v[178:179], v[188:189], 0, v[112:113]
	global_load_dwordx2 v[202:203], v[178:179], off
	global_load_dwordx2 v[196:197], v[178:179], off offset:512
	global_load_dwordx2 v[188:189], v[178:179], off offset:1024
	global_load_dwordx2 v[182:183], v[178:179], off offset:1536
	s_mov_b32 s97, 1
.Lp1pf_skip:
	s_waitcnt lgkmcnt(0)
	s_barrier
	v_add_u32_e32 v108, 0x10200, v241
	ds_read_b128 v[80:83], v108
	ds_read_b128 v[84:87], v241
	ds_read_b128 v[88:91], v108 offset:64
	ds_read_b128 v[92:95], v241 offset:64
	ds_read_b128 v[100:103], v241 offset:33024
	ds_read_b128 v[104:107], v241 offset:33088
	s_waitcnt lgkmcnt(4)
	v_mfma_f32_16x16x32_bf16 v[96:99], v[80:83], v[84:87], 0
	v_add_u32_e32 v109, 0x18300, v241
	s_mov_b32 s2, 0x9000
	s_waitcnt lgkmcnt(1)
	v_mfma_f32_16x16x32_bf16 v[80:83], v[80:83], v[100:103], v[96:99]
	s_nop 3
	ds_read_b128 v[96:99], v109
	ds_read_b128 v[100:103], v109 offset:64
	s_waitcnt lgkmcnt(1)
	v_mfma_f32_16x16x32_bf16 v[80:83], v[96:99], v[84:87], v[80:83]
	ds_read_b128 v[84:87], v108 offset:128
	v_mfma_f32_16x16x32_bf16 v[80:83], v[88:91], v[92:95], v[80:83]
	v_mfma_f32_16x16x32_bf16 v[80:83], v[88:91], v[104:107], v[80:83]
	s_waitcnt lgkmcnt(1)
	v_mfma_f32_16x16x32_bf16 v[80:83], v[100:103], v[92:95], v[80:83]
	ds_read_b128 v[88:91], v241 offset:128
	ds_read_b128 v[92:95], v108 offset:192
	ds_read_b128 v[96:99], v241 offset:192
	ds_read_b128 v[100:103], v241 offset:33152
	ds_read_b128 v[104:107], v241 offset:33216
	s_waitcnt lgkmcnt(4)
	v_mfma_f32_16x16x32_bf16 v[80:83], v[84:87], v[88:91], v[80:83]
	s_waitcnt lgkmcnt(1)
	v_mfma_f32_16x16x32_bf16 v[80:83], v[84:87], v[100:103], v[80:83]
	ds_read_b128 v[84:87], v109 offset:128
	ds_read_b128 v[100:103], v109 offset:192
	s_waitcnt lgkmcnt(1)
	v_mfma_f32_16x16x32_bf16 v[80:83], v[84:87], v[88:91], v[80:83]
	v_mfma_f32_16x16x32_bf16 v[80:83], v[92:95], v[96:99], v[80:83]
	v_mfma_f32_16x16x32_bf16 v[80:83], v[92:95], v[104:107], v[80:83]
	s_waitcnt lgkmcnt(0)
	v_mfma_f32_16x16x32_bf16 v[80:83], v[100:103], v[96:99], v[80:83]
	s_nop 7
	ds_write2_b32 v242, v80, v81 offset1:16
	ds_write2_b32 v242, v82, v83 offset0:32 offset1:48
	s_waitcnt lgkmcnt(0)
	s_barrier
	v_add_u32_e32 v80, s21, v237
	v_cmp_gt_i32_e32 vcc, s2, v80
	s_and_b64 s[4:5], s[56:57], vcc
	s_and_saveexec_b64 s[2:3], s[4:5]
	s_cbranch_execz .LBB0_142
	global_load_dword v81, v[138:139], off
	ds_read2st64_b32 v[82:83], v238 offset1:4
	ds_read2st64_b32 v[84:85], v238 offset0:8 offset1:12
	ds_read2st64_b32 v[86:87], v238 offset0:16 offset1:20
	ds_read2st64_b32 v[88:89], v238 offset0:24 offset1:28
	s_mov_b32 s4, 0xbfb8aa3b
	s_waitcnt lgkmcnt(3)
	v_add_f32_e32 v82, 0, v82
	v_add_f32_e32 v82, v82, v83
	s_waitcnt lgkmcnt(2)
	v_add_f32_e32 v82, v82, v84
	v_add_f32_e32 v82, v82, v85
	s_waitcnt lgkmcnt(1)
	v_add_f32_e32 v82, v82, v86
	v_add_f32_e32 v82, v82, v87
	s_waitcnt lgkmcnt(0)
	v_add_f32_e32 v82, v82, v88
	v_add_f32_e32 v82, v82, v89
	v_mov_b32_e32 v87, 0x41b17218
	s_waitcnt vmcnt(0)
	v_add_f32_e32 v82, v82, v81
	v_mul_f32_e64 v81, |v82|, s4
	v_exp_f32_e32 v83, v81
	s_mov_b32 s4, 0x3f317217
	v_ashrrev_i32_e32 v81, 31, v80
	v_lshlrev_b64 v[80:81], 6, v[80:81]
	v_add_f32_e32 v84, 1.0, v83
	v_cmp_gt_f32_e32 vcc, s22, v84
	v_add_f32_e32 v86, -1.0, v84
	v_rcp_f32_e32 v86, v86
	v_cndmask_b32_e64 v85, 0, 32, vcc
	v_ldexp_f32 v85, v84, v85
	v_log_f32_e32 v85, v85
	v_cndmask_b32_e32 v87, 0, v87, vcc
	v_mul_f32_e32 v86, v83, v86
	v_max_f32_e32 v82, 0, v82
	v_mul_f32_e32 v88, 0x3f317217, v85
	v_fma_f32 v88, v85, s4, -v88
	v_fmac_f32_e32 v88, 0x3377d1cf, v85
	s_mov_b32 s4, 0x7f800000
	v_fmac_f32_e32 v88, 0x3f317217, v85
	v_cmp_lt_f32_e64 vcc, |v85|, s4
	v_lshl_add_u64 v[80:81], v[140:141], 0, v[80:81]
	s_nop 0
	v_cndmask_b32_e32 v85, v85, v88, vcc
	v_sub_f32_e32 v85, v85, v87
	v_mul_f32_e32 v85, v85, v86
	v_cmp_eq_f32_e32 vcc, 1.0, v84
	s_nop 1
	v_cndmask_b32_e32 v83, v85, v83, vcc
	v_add_f32_e32 v82, v82, v83
	global_store_dword v[80:81], v82, off
	s_branch .LBB0_142
